# LSTM gate math: the four 1+exp adds as two v_pk_add_f32, running-max update moved into the trans->VALU wait slot (3 fewer issue slots per step); on top of the prologue-trimmed MP kernels
# speedup vs baseline: 1.0077x; 1.0044x over previous
.Llstm3_loop:
	ds_read_b128 v[184:187], v209 offset:0
	ds_read_b128 v[188:191], v209 offset:64
	ds_read_b128 v[176:179], v211 offset:0
	ds_read_b128 v[180:183], v211 offset:64
	v_mfma_f32_16x16x32_f16 v[164:167], v[68:71], v[148:151], v[164:167]
	s_waitcnt vmcnt(4)
	v_mfma_f32_16x16x32_f16 v[160:163], v[60:63], v[156:159], v[160:163]
	s_waitcnt lgkmcnt(3)
	v_mfma_f32_16x16x32_f16 v[168:171], v[16:19], v[184:187], v[192:195]
	v_mfma_f32_16x16x32_f16 v[172:175], v[24:27], v[184:187], v[192:195]
	s_waitcnt lgkmcnt(2)
	v_mfma_f32_16x16x32_f16 v[168:171], v[20:23], v[188:191], v[168:171]
	v_mfma_f32_16x16x32_f16 v[172:175], v[28:31], v[188:191], v[172:175]
	s_waitcnt lgkmcnt(1)
	v_mfma_f32_16x16x32_f16 v[168:171], v[32:35], v[176:179], v[168:171]
	v_mfma_f32_16x16x32_f16 v[172:175], v[40:43], v[176:179], v[172:175]
	s_waitcnt lgkmcnt(0)
	v_mfma_f32_16x16x32_f16 v[168:171], v[36:39], v[180:183], v[168:171]
	v_mfma_f32_16x16x32_f16 v[172:175], v[44:47], v[180:183], v[172:175]
	s_nop 7
	v_mov_b32_dpp v168, v172 quad_perm:[0,1,2,3] row_mask:0xf bank_mask:0xa
	v_mov_b32_dpp v169, v173 quad_perm:[0,1,2,3] row_mask:0xf bank_mask:0xa
	v_mov_b32_dpp v170, v174 quad_perm:[0,1,2,3] row_mask:0xf bank_mask:0xa
	v_exp_f32_e32 v200, v168
	v_mov_b32_dpp v171, v175 quad_perm:[0,1,2,3] row_mask:0xf bank_mask:0xa
	v_exp_f32_e32 v201, v169
	v_exp_f32_e32 v202, v170
	v_exp_f32_e32 v203, v171
	v_pk_add_f32 v[200:201], v[200:201], 1.0 op_sel_hi:[1,0]
	v_pk_add_f32 v[202:203], v[202:203], 1.0 op_sel_hi:[1,0]
	v_rcp_f32_e32 v202, v202
	v_rcp_f32_e32 v200, v200
	v_rcp_f32_e32 v201, v201
	v_rcp_f32_e32 v203, v203
	v_fmamk_f32 v204, v202, 0xc0b8aa3b, v222
	v_mul_f32_e32 v205, v200, v204
	v_fma_f32 v220, v201, v220, v205
	v_exp_f32_e32 v206, v220
	v_mul_f32_e32 v207, -2.0, v203
	v_add_f32_e32 v206, 1.0, v206
	v_rcp_f32_e32 v206, v206
	v_max_f32_e32 v221, v221, v215
	v_fma_mixlo_f16 v208, v206, v207, v203
	ds_write_b16 v225, v208 offset:576
	v_fma_f32 v215, v206, v207, v203
	v_mfma_f32_16x16x32_f16 v[232:235], v[80:83], v[144:147], v[120:123]
	v_mfma_f32_16x16x32_f16 v[164:167], v[72:75], v[152:155], v[164:167]
	ds_write_b128 v227, v[160:163] offset:4352
	ds_read_b128 v[196:199], v226 offset:1088
	s_waitcnt lgkmcnt(2)
	s_barrier
	ds_read_b128 v[184:187], v210 offset:576
	ds_read_b128 v[188:191], v210 offset:640
	ds_read_b128 v[176:179], v212 offset:576
	ds_read_b128 v[180:183], v212 offset:640
	v_mfma_f32_16x16x32_f16 v[232:235], v[84:87], v[148:151], v[232:235]
	v_mfma_f32_16x16x32_f16 v[164:167], v[76:79], v[156:159], v[164:167]
	s_waitcnt lgkmcnt(3)
	v_mfma_f32_16x16x32_f16 v[168:171], v[16:19], v[184:187], v[196:199]
	v_mfma_f32_16x16x32_f16 v[172:175], v[24:27], v[184:187], v[196:199]
	s_waitcnt lgkmcnt(2)
	v_mfma_f32_16x16x32_f16 v[168:171], v[20:23], v[188:191], v[168:171]
	v_mfma_f32_16x16x32_f16 v[172:175], v[28:31], v[188:191], v[172:175]
	s_waitcnt lgkmcnt(1)
	v_mfma_f32_16x16x32_f16 v[168:171], v[32:35], v[176:179], v[168:171]
	v_mfma_f32_16x16x32_f16 v[172:175], v[40:43], v[176:179], v[172:175]
	s_waitcnt lgkmcnt(0)
	v_mfma_f32_16x16x32_f16 v[168:171], v[36:39], v[180:183], v[168:171]
	v_mfma_f32_16x16x32_f16 v[172:175], v[44:47], v[180:183], v[172:175]
	s_nop 7
	v_mov_b32_dpp v168, v172 quad_perm:[0,1,2,3] row_mask:0xf bank_mask:0xa
	v_mov_b32_dpp v169, v173 quad_perm:[0,1,2,3] row_mask:0xf bank_mask:0xa
	v_mov_b32_dpp v170, v174 quad_perm:[0,1,2,3] row_mask:0xf bank_mask:0xa
	v_exp_f32_e32 v200, v168
	v_mov_b32_dpp v171, v175 quad_perm:[0,1,2,3] row_mask:0xf bank_mask:0xa
	v_exp_f32_e32 v201, v169
	v_exp_f32_e32 v202, v170
	v_exp_f32_e32 v203, v171
	v_pk_add_f32 v[200:201], v[200:201], 1.0 op_sel_hi:[1,0]
	v_pk_add_f32 v[202:203], v[202:203], 1.0 op_sel_hi:[1,0]
	v_rcp_f32_e32 v202, v202
	v_rcp_f32_e32 v200, v200
	v_rcp_f32_e32 v201, v201
	v_rcp_f32_e32 v203, v203
	v_fmamk_f32 v204, v202, 0xc0b8aa3b, v222
	v_mul_f32_e32 v205, v200, v204
	v_fma_f32 v220, v201, v220, v205
	v_exp_f32_e32 v206, v220
	v_mul_f32_e32 v207, -2.0, v203
	v_add_f32_e32 v206, 1.0, v206
	v_rcp_f32_e32 v206, v206
	v_max_f32_e32 v221, v221, v215
	v_fma_mixlo_f16 v208, v206, v207, v203
	ds_write_b16 v225, v208 offset:0
	v_fma_f32 v215, v206, v207, v203
	v_mfma_f32_16x16x32_f16 v[236:239], v[96:99], v[144:147], v[124:127]
	v_mfma_f32_16x16x32_f16 v[232:235], v[88:91], v[152:155], v[232:235]
	global_load_dwordx4 v[144:147], v[228:229], off offset:0
	ds_write_b128 v227, v[164:167] offset:4416
	ds_read_b128 v[192:195], v226 offset:2176
	s_waitcnt lgkmcnt(2)
	s_barrier
	ds_read_b128 v[184:187], v209 offset:0
	ds_read_b128 v[188:191], v209 offset:64
	ds_read_b128 v[176:179], v211 offset:0
	ds_read_b128 v[180:183], v211 offset:64
	v_mfma_f32_16x16x32_f16 v[236:239], v[100:103], v[148:151], v[236:239]
	v_mfma_f32_16x16x32_f16 v[232:235], v[92:95], v[156:159], v[232:235]
	global_load_dwordx4 v[148:151], v[228:229], off offset:64
	s_waitcnt lgkmcnt(3)
	v_mfma_f32_16x16x32_f16 v[168:171], v[16:19], v[184:187], v[192:195]
	v_mfma_f32_16x16x32_f16 v[172:175], v[24:27], v[184:187], v[192:195]
	s_waitcnt lgkmcnt(2)
	v_mfma_f32_16x16x32_f16 v[168:171], v[20:23], v[188:191], v[168:171]
	v_mfma_f32_16x16x32_f16 v[172:175], v[28:31], v[188:191], v[172:175]
	s_waitcnt lgkmcnt(1)
	v_mfma_f32_16x16x32_f16 v[168:171], v[32:35], v[176:179], v[168:171]
	v_mfma_f32_16x16x32_f16 v[172:175], v[40:43], v[176:179], v[172:175]
	s_waitcnt lgkmcnt(0)
	v_mfma_f32_16x16x32_f16 v[168:171], v[36:39], v[180:183], v[168:171]
	v_mfma_f32_16x16x32_f16 v[172:175], v[44:47], v[180:183], v[172:175]
	s_nop 7
	v_mov_b32_dpp v168, v172 quad_perm:[0,1,2,3] row_mask:0xf bank_mask:0xa
	v_mov_b32_dpp v169, v173 quad_perm:[0,1,2,3] row_mask:0xf bank_mask:0xa
	v_mov_b32_dpp v170, v174 quad_perm:[0,1,2,3] row_mask:0xf bank_mask:0xa
	v_exp_f32_e32 v200, v168
	v_mov_b32_dpp v171, v175 quad_perm:[0,1,2,3] row_mask:0xf bank_mask:0xa
	v_exp_f32_e32 v201, v169
	v_exp_f32_e32 v202, v170
	v_exp_f32_e32 v203, v171
	v_pk_add_f32 v[200:201], v[200:201], 1.0 op_sel_hi:[1,0]
	v_pk_add_f32 v[202:203], v[202:203], 1.0 op_sel_hi:[1,0]
	v_rcp_f32_e32 v202, v202
	v_rcp_f32_e32 v200, v200
	v_rcp_f32_e32 v201, v201
	v_rcp_f32_e32 v203, v203
	v_fmamk_f32 v204, v202, 0xc0b8aa3b, v222
	v_mul_f32_e32 v205, v200, v204
	v_fma_f32 v220, v201, v220, v205
	v_exp_f32_e32 v206, v220
	v_mul_f32_e32 v207, -2.0, v203
	v_add_f32_e32 v206, 1.0, v206
	v_rcp_f32_e32 v206, v206
	v_max_f32_e32 v221, v221, v215
	v_fma_mixlo_f16 v208, v206, v207, v203
	ds_write_b16 v225, v208 offset:576
	v_fma_f32 v215, v206, v207, v203
	s_waitcnt vmcnt(5)
	v_mfma_f32_16x16x32_f16 v[160:163], v[48:51], v[128:131], v[112:115]
	v_mfma_f32_16x16x32_f16 v[236:239], v[104:107], v[152:155], v[236:239]
	global_load_dwordx4 v[152:155], v[228:229], off offset:128
	ds_write_b128 v227, v[232:235] offset:4480
	ds_read_b128 v[196:199], v226 offset:3264
	s_waitcnt lgkmcnt(2)
	s_barrier
	ds_read_b128 v[184:187], v210 offset:576
	ds_read_b128 v[188:191], v210 offset:640
	ds_read_b128 v[176:179], v212 offset:576
	ds_read_b128 v[180:183], v212 offset:640
	s_waitcnt vmcnt(5)
	v_mfma_f32_16x16x32_f16 v[160:163], v[52:55], v[132:135], v[160:163]
	v_mfma_f32_16x16x32_f16 v[236:239], v[108:111], v[156:159], v[236:239]
	global_load_dwordx4 v[156:159], v[228:229], off offset:192
	v_lshl_add_u64 v[228:229], v[228:229], 0, s[20:21]
	s_waitcnt lgkmcnt(3)
	v_mfma_f32_16x16x32_f16 v[168:171], v[16:19], v[184:187], v[196:199]
	v_mfma_f32_16x16x32_f16 v[172:175], v[24:27], v[184:187], v[196:199]
	s_waitcnt lgkmcnt(2)
	v_mfma_f32_16x16x32_f16 v[168:171], v[20:23], v[188:191], v[168:171]
	v_mfma_f32_16x16x32_f16 v[172:175], v[28:31], v[188:191], v[172:175]
	s_waitcnt lgkmcnt(1)
	v_mfma_f32_16x16x32_f16 v[168:171], v[32:35], v[176:179], v[168:171]
	v_mfma_f32_16x16x32_f16 v[172:175], v[40:43], v[176:179], v[172:175]
	s_waitcnt lgkmcnt(0)
	v_mfma_f32_16x16x32_f16 v[168:171], v[36:39], v[180:183], v[168:171]
	v_mfma_f32_16x16x32_f16 v[172:175], v[44:47], v[180:183], v[172:175]
	s_nop 7
	v_mov_b32_dpp v168, v172 quad_perm:[0,1,2,3] row_mask:0xf bank_mask:0xa
	v_mov_b32_dpp v169, v173 quad_perm:[0,1,2,3] row_mask:0xf bank_mask:0xa
	v_mov_b32_dpp v170, v174 quad_perm:[0,1,2,3] row_mask:0xf bank_mask:0xa
	v_exp_f32_e32 v200, v168
	v_mov_b32_dpp v171, v175 quad_perm:[0,1,2,3] row_mask:0xf bank_mask:0xa
	v_exp_f32_e32 v201, v169
	v_exp_f32_e32 v202, v170
	v_exp_f32_e32 v203, v171
	v_pk_add_f32 v[200:201], v[200:201], 1.0 op_sel_hi:[1,0]
	v_pk_add_f32 v[202:203], v[202:203], 1.0 op_sel_hi:[1,0]
	v_rcp_f32_e32 v202, v202
	v_rcp_f32_e32 v200, v200
	v_rcp_f32_e32 v201, v201
	v_rcp_f32_e32 v203, v203
	v_fmamk_f32 v204, v202, 0xc0b8aa3b, v222
	v_mul_f32_e32 v205, v200, v204
	v_fma_f32 v220, v201, v220, v205
	v_exp_f32_e32 v206, v220
	v_mul_f32_e32 v207, -2.0, v203
	v_add_f32_e32 v206, 1.0, v206
	v_rcp_f32_e32 v206, v206
	v_max_f32_e32 v221, v221, v215
	v_fma_mixlo_f16 v208, v206, v207, v203
	ds_write_b16 v225, v208 offset:0
	v_fma_f32 v215, v206, v207, v203
	v_mfma_f32_16x16x32_f16 v[164:167], v[64:67], v[128:131], v[116:119]
	s_waitcnt vmcnt(5)
	v_mfma_f32_16x16x32_f16 v[160:163], v[56:59], v[136:139], v[160:163]
	ds_write_b128 v227, v[236:239] offset:4544
	ds_read_b128 v[192:195], v226 offset:4352
	s_waitcnt lgkmcnt(2)
	s_barrier
	ds_read_b128 v[184:187], v209 offset:0
	ds_read_b128 v[188:191], v209 offset:64
	ds_read_b128 v[176:179], v211 offset:0
	ds_read_b128 v[180:183], v211 offset:64
	v_mfma_f32_16x16x32_f16 v[164:167], v[68:71], v[132:135], v[164:167]
	s_waitcnt vmcnt(4)
	v_mfma_f32_16x16x32_f16 v[160:163], v[60:63], v[140:143], v[160:163]
	s_waitcnt lgkmcnt(3)
	v_mfma_f32_16x16x32_f16 v[168:171], v[16:19], v[184:187], v[192:195]
	v_mfma_f32_16x16x32_f16 v[172:175], v[24:27], v[184:187], v[192:195]
	s_waitcnt lgkmcnt(2)
	v_mfma_f32_16x16x32_f16 v[168:171], v[20:23], v[188:191], v[168:171]
	v_mfma_f32_16x16x32_f16 v[172:175], v[28:31], v[188:191], v[172:175]
	s_waitcnt lgkmcnt(1)
	v_mfma_f32_16x16x32_f16 v[168:171], v[32:35], v[176:179], v[168:171]
	v_mfma_f32_16x16x32_f16 v[172:175], v[40:43], v[176:179], v[172:175]
	s_waitcnt lgkmcnt(0)
	v_mfma_f32_16x16x32_f16 v[168:171], v[36:39], v[180:183], v[168:171]
	v_mfma_f32_16x16x32_f16 v[172:175], v[44:47], v[180:183], v[172:175]
	s_nop 7
	v_mov_b32_dpp v168, v172 quad_perm:[0,1,2,3] row_mask:0xf bank_mask:0xa
	v_mov_b32_dpp v169, v173 quad_perm:[0,1,2,3] row_mask:0xf bank_mask:0xa
	v_mov_b32_dpp v170, v174 quad_perm:[0,1,2,3] row_mask:0xf bank_mask:0xa
	v_exp_f32_e32 v200, v168
	v_mov_b32_dpp v171, v175 quad_perm:[0,1,2,3] row_mask:0xf bank_mask:0xa
	v_exp_f32_e32 v201, v169
	v_exp_f32_e32 v202, v170
	v_exp_f32_e32 v203, v171
	v_pk_add_f32 v[200:201], v[200:201], 1.0 op_sel_hi:[1,0]
	v_pk_add_f32 v[202:203], v[202:203], 1.0 op_sel_hi:[1,0]
	v_rcp_f32_e32 v202, v202
	v_rcp_f32_e32 v200, v200
	v_rcp_f32_e32 v201, v201
	v_rcp_f32_e32 v203, v203
	v_fmamk_f32 v204, v202, 0xc0b8aa3b, v222
	v_mul_f32_e32 v205, v200, v204
	v_fma_f32 v220, v201, v220, v205
	v_exp_f32_e32 v206, v220
	v_mul_f32_e32 v207, -2.0, v203
	v_add_f32_e32 v206, 1.0, v206
	v_rcp_f32_e32 v206, v206
	v_max_f32_e32 v221, v221, v215
	v_fma_mixlo_f16 v208, v206, v207, v203
	ds_write_b16 v225, v208 offset:576
	v_fma_f32 v215, v206, v207, v203
	v_mfma_f32_16x16x32_f16 v[232:235], v[80:83], v[128:131], v[120:123]
	v_mfma_f32_16x16x32_f16 v[164:167], v[72:75], v[136:139], v[164:167]
	ds_write_b128 v227, v[160:163] offset:0
	ds_read_b128 v[196:199], v226 offset:5440
	s_waitcnt lgkmcnt(2)
	s_barrier
	ds_read_b128 v[184:187], v210 offset:576
	ds_read_b128 v[188:191], v210 offset:640
	ds_read_b128 v[176:179], v212 offset:576
	ds_read_b128 v[180:183], v212 offset:640
	v_mfma_f32_16x16x32_f16 v[232:235], v[84:87], v[132:135], v[232:235]
	v_mfma_f32_16x16x32_f16 v[164:167], v[76:79], v[140:143], v[164:167]
	s_waitcnt lgkmcnt(3)
	v_mfma_f32_16x16x32_f16 v[168:171], v[16:19], v[184:187], v[196:199]
	v_mfma_f32_16x16x32_f16 v[172:175], v[24:27], v[184:187], v[196:199]
	s_waitcnt lgkmcnt(2)
	v_mfma_f32_16x16x32_f16 v[168:171], v[20:23], v[188:191], v[168:171]
	v_mfma_f32_16x16x32_f16 v[172:175], v[28:31], v[188:191], v[172:175]
	s_waitcnt lgkmcnt(1)
	v_mfma_f32_16x16x32_f16 v[168:171], v[32:35], v[176:179], v[168:171]
	v_mfma_f32_16x16x32_f16 v[172:175], v[40:43], v[176:179], v[172:175]
	s_waitcnt lgkmcnt(0)
	v_mfma_f32_16x16x32_f16 v[168:171], v[36:39], v[180:183], v[168:171]
	v_mfma_f32_16x16x32_f16 v[172:175], v[44:47], v[180:183], v[172:175]
	s_nop 7
	v_mov_b32_dpp v168, v172 quad_perm:[0,1,2,3] row_mask:0xf bank_mask:0xa
	v_mov_b32_dpp v169, v173 quad_perm:[0,1,2,3] row_mask:0xf bank_mask:0xa
	v_mov_b32_dpp v170, v174 quad_perm:[0,1,2,3] row_mask:0xf bank_mask:0xa
	v_exp_f32_e32 v200, v168
	v_mov_b32_dpp v171, v175 quad_perm:[0,1,2,3] row_mask:0xf bank_mask:0xa
	v_exp_f32_e32 v201, v169
	v_exp_f32_e32 v202, v170
	v_exp_f32_e32 v203, v171
	v_pk_add_f32 v[200:201], v[200:201], 1.0 op_sel_hi:[1,0]
	v_pk_add_f32 v[202:203], v[202:203], 1.0 op_sel_hi:[1,0]
	v_rcp_f32_e32 v202, v202
	v_rcp_f32_e32 v200, v200
	v_rcp_f32_e32 v201, v201
	v_rcp_f32_e32 v203, v203
	v_fmamk_f32 v204, v202, 0xc0b8aa3b, v222
	v_mul_f32_e32 v205, v200, v204
	v_fma_f32 v220, v201, v220, v205
	v_exp_f32_e32 v206, v220
	v_mul_f32_e32 v207, -2.0, v203
	v_add_f32_e32 v206, 1.0, v206
	v_rcp_f32_e32 v206, v206
	v_max_f32_e32 v221, v221, v215
	v_fma_mixlo_f16 v208, v206, v207, v203
	ds_write_b16 v225, v208 offset:0
	v_fma_f32 v215, v206, v207, v203
	v_mfma_f32_16x16x32_f16 v[236:239], v[96:99], v[128:131], v[124:127]
	v_mfma_f32_16x16x32_f16 v[232:235], v[88:91], v[136:139], v[232:235]
	global_load_dwordx4 v[128:131], v[228:229], off offset:0
	ds_write_b128 v227, v[164:167] offset:64
	ds_read_b128 v[192:195], v226 offset:6528
	s_waitcnt lgkmcnt(2)
	s_barrier
	ds_read_b128 v[184:187], v209 offset:0
	ds_read_b128 v[188:191], v209 offset:64
	ds_read_b128 v[176:179], v211 offset:0
	ds_read_b128 v[180:183], v211 offset:64
	v_mfma_f32_16x16x32_f16 v[236:239], v[100:103], v[132:135], v[236:239]
	v_mfma_f32_16x16x32_f16 v[232:235], v[92:95], v[140:143], v[232:235]
	global_load_dwordx4 v[132:135], v[228:229], off offset:64
	s_waitcnt lgkmcnt(3)
	v_mfma_f32_16x16x32_f16 v[168:171], v[16:19], v[184:187], v[192:195]
	v_mfma_f32_16x16x32_f16 v[172:175], v[24:27], v[184:187], v[192:195]
	s_waitcnt lgkmcnt(2)
	v_mfma_f32_16x16x32_f16 v[168:171], v[20:23], v[188:191], v[168:171]
	v_mfma_f32_16x16x32_f16 v[172:175], v[28:31], v[188:191], v[172:175]
	s_waitcnt lgkmcnt(1)
	v_mfma_f32_16x16x32_f16 v[168:171], v[32:35], v[176:179], v[168:171]
	v_mfma_f32_16x16x32_f16 v[172:175], v[40:43], v[176:179], v[172:175]
	s_waitcnt lgkmcnt(0)
	v_mfma_f32_16x16x32_f16 v[168:171], v[36:39], v[180:183], v[168:171]
	v_mfma_f32_16x16x32_f16 v[172:175], v[44:47], v[180:183], v[172:175]
	s_nop 7
	v_mov_b32_dpp v168, v172 quad_perm:[0,1,2,3] row_mask:0xf bank_mask:0xa
	v_mov_b32_dpp v169, v173 quad_perm:[0,1,2,3] row_mask:0xf bank_mask:0xa
	v_mov_b32_dpp v170, v174 quad_perm:[0,1,2,3] row_mask:0xf bank_mask:0xa
	v_exp_f32_e32 v200, v168
	v_mov_b32_dpp v171, v175 quad_perm:[0,1,2,3] row_mask:0xf bank_mask:0xa
	v_exp_f32_e32 v201, v169
	v_exp_f32_e32 v202, v170
	v_exp_f32_e32 v203, v171
	v_pk_add_f32 v[200:201], v[200:201], 1.0 op_sel_hi:[1,0]
	v_pk_add_f32 v[202:203], v[202:203], 1.0 op_sel_hi:[1,0]
	v_rcp_f32_e32 v202, v202
	v_rcp_f32_e32 v200, v200
	v_rcp_f32_e32 v201, v201
	v_rcp_f32_e32 v203, v203
	v_fmamk_f32 v204, v202, 0xc0b8aa3b, v222
	v_mul_f32_e32 v205, v200, v204
	v_fma_f32 v220, v201, v220, v205
	v_exp_f32_e32 v206, v220
	v_mul_f32_e32 v207, -2.0, v203
	v_add_f32_e32 v206, 1.0, v206
	v_rcp_f32_e32 v206, v206
	v_max_f32_e32 v221, v221, v215
	v_fma_mixlo_f16 v208, v206, v207, v203
	ds_write_b16 v225, v208 offset:576
	v_fma_f32 v215, v206, v207, v203
	s_waitcnt vmcnt(5)
	v_mfma_f32_16x16x32_f16 v[160:163], v[48:51], v[144:147], v[112:115]
	v_mfma_f32_16x16x32_f16 v[236:239], v[104:107], v[136:139], v[236:239]
	global_load_dwordx4 v[136:139], v[228:229], off offset:128
	ds_write_b128 v227, v[232:235] offset:128
	ds_read_b128 v[196:199], v226 offset:7616
	s_waitcnt lgkmcnt(2)
	s_barrier
	ds_read_b128 v[184:187], v210 offset:576
	ds_read_b128 v[188:191], v210 offset:640
	ds_read_b128 v[176:179], v212 offset:576
	ds_read_b128 v[180:183], v212 offset:640
	s_waitcnt vmcnt(5)
	v_mfma_f32_16x16x32_f16 v[160:163], v[52:55], v[148:151], v[160:163]
	v_mfma_f32_16x16x32_f16 v[236:239], v[108:111], v[140:143], v[236:239]
	global_load_dwordx4 v[140:143], v[228:229], off offset:192
	v_lshl_add_u64 v[228:229], v[228:229], 0, s[20:21]
	s_waitcnt lgkmcnt(3)
	v_mfma_f32_16x16x32_f16 v[168:171], v[16:19], v[184:187], v[196:199]
	v_mfma_f32_16x16x32_f16 v[172:175], v[24:27], v[184:187], v[196:199]
	s_waitcnt lgkmcnt(2)
	v_mfma_f32_16x16x32_f16 v[168:171], v[20:23], v[188:191], v[168:171]
	v_mfma_f32_16x16x32_f16 v[172:175], v[28:31], v[188:191], v[172:175]
	s_waitcnt lgkmcnt(1)
	v_mfma_f32_16x16x32_f16 v[168:171], v[32:35], v[176:179], v[168:171]
	v_mfma_f32_16x16x32_f16 v[172:175], v[40:43], v[176:179], v[172:175]
	s_waitcnt lgkmcnt(0)
	v_mfma_f32_16x16x32_f16 v[168:171], v[36:39], v[180:183], v[168:171]
	v_mfma_f32_16x16x32_f16 v[172:175], v[44:47], v[180:183], v[172:175]
	s_nop 7
	v_mov_b32_dpp v168, v172 quad_perm:[0,1,2,3] row_mask:0xf bank_mask:0xa
	v_mov_b32_dpp v169, v173 quad_perm:[0,1,2,3] row_mask:0xf bank_mask:0xa
	v_mov_b32_dpp v170, v174 quad_perm:[0,1,2,3] row_mask:0xf bank_mask:0xa
	v_exp_f32_e32 v200, v168
	v_mov_b32_dpp v171, v175 quad_perm:[0,1,2,3] row_mask:0xf bank_mask:0xa
	v_exp_f32_e32 v201, v169
	v_exp_f32_e32 v202, v170
	v_exp_f32_e32 v203, v171
	v_pk_add_f32 v[200:201], v[200:201], 1.0 op_sel_hi:[1,0]
	v_pk_add_f32 v[202:203], v[202:203], 1.0 op_sel_hi:[1,0]
	v_rcp_f32_e32 v202, v202
	v_rcp_f32_e32 v200, v200
	v_rcp_f32_e32 v201, v201
	v_rcp_f32_e32 v203, v203
	v_fmamk_f32 v204, v202, 0xc0b8aa3b, v222
	v_mul_f32_e32 v205, v200, v204
	v_fma_f32 v220, v201, v220, v205
	v_exp_f32_e32 v206, v220
	v_mul_f32_e32 v207, -2.0, v203
	v_add_f32_e32 v206, 1.0, v206
	v_rcp_f32_e32 v206, v206
	v_max_f32_e32 v221, v221, v215
	v_fma_mixlo_f16 v208, v206, v207, v203
	ds_write_b16 v225, v208 offset:0
	v_fma_f32 v215, v206, v207, v203
	v_mfma_f32_16x16x32_f16 v[164:167], v[64:67], v[144:147], v[116:119]
	s_waitcnt vmcnt(5)
	v_mfma_f32_16x16x32_f16 v[160:163], v[56:59], v[152:155], v[160:163]
	ds_write_b128 v227, v[236:239] offset:192
	ds_read_b128 v[192:195], v226 offset:0
	s_waitcnt lgkmcnt(2)
	s_barrier
	s_sub_u32 s4, s4, 1
	s_cmp_lg_u32 s4, 0
	s_cbranch_scc1 .Llstm3_loop
	v_max_f32_e32 v221, v221, v215
	global_store_dword v230, v221, s[12:13]
	s_endpgm
